# C1 + P7 mid-hook and final-epilogue second-half gate loads issued with the first half (no store drain before them)
# baseline (speedup 1.0000x reference)
.LBB0_962:
	s_cmpk_lg_i32 s58, 0x900
	s_cbranch_scc1 .LBB0_961
	v_mov_b32_e32 v3, 0
	v_mov_b32_e32 v132, 0
	v_add_u32_e32 v3, v3, v194
	v_add_lshl_u32 v132, v132, v1, 3
	v_add_u32_e32 v154, s31, v3
	v_ashrrev_i32_e32 v133, 31, v132
	v_ashrrev_i32_e32 v155, 31, v154
	v_lshl_add_u64 v[132:133], v[132:133], 1, s[56:57]
	v_lshlrev_b64 v[134:135], 12, v[154:155]
	v_add_u32_e32 v142, 16, v154
	v_add_u32_e32 v150, 32, v154
	v_lshl_add_u64 v[138:139], v[132:133], 0, v[134:135]
	v_ashrrev_i32_e32 v143, 31, v142
	v_ashrrev_i32_e32 v151, 31, v150
	global_load_dwordx4 v[134:137], v[138:139], off
	s_nop 0
	global_load_dwordx4 v[138:141], v[138:139], off offset:256
	v_lshlrev_b64 v[142:143], 12, v[142:143]
	v_lshlrev_b64 v[150:151], 12, v[150:151]
	v_add_u32_e32 v154, 48, v154
	v_lshl_add_u64 v[146:147], v[132:133], 0, v[142:143]
	v_lshl_add_u64 v[176:177], v[132:133], 0, v[150:151]
	v_ashrrev_i32_e32 v155, 31, v154
	global_load_dwordx4 v[142:145], v[146:147], off
	s_nop 0
	global_load_dwordx4 v[146:149], v[146:147], off offset:256
	s_nop 0
	global_load_dwordx4 v[150:153], v[176:177], off
	s_nop 0
	global_load_dwordx4 v[176:179], v[176:177], off offset:256
	v_lshlrev_b64 v[154:155], 12, v[154:155]
	v_lshl_add_u64 v[154:155], v[132:133], 0, v[154:155]
	global_load_dwordx4 v[180:183], v[154:155], off
	global_load_dwordx4 v[184:187], v[154:155], off offset:256
	v_add_u32_e32 v232, s83, v3
	v_ashrrev_i32_e32 v233, 31, v232
	v_lshlrev_b64 v[234:235], 12, v[232:233]
	v_lshl_add_u64 v[234:235], v[132:133], 0, v[234:235]
	global_load_dwordx4 v[200:203], v[234:235], off
	global_load_dwordx4 v[204:207], v[234:235], off offset:256
	v_add_u32_e32 v232, 16, v232
	v_ashrrev_i32_e32 v233, 31, v232
	v_lshlrev_b64 v[234:235], 12, v[232:233]
	v_lshl_add_u64 v[234:235], v[132:133], 0, v[234:235]
	global_load_dwordx4 v[208:211], v[234:235], off
	global_load_dwordx4 v[212:215], v[234:235], off offset:256
	v_add_u32_e32 v232, 16, v232
	v_ashrrev_i32_e32 v233, 31, v232
	v_lshlrev_b64 v[234:235], 12, v[232:233]
	v_lshl_add_u64 v[234:235], v[132:133], 0, v[234:235]
	global_load_dwordx4 v[216:219], v[234:235], off
	global_load_dwordx4 v[220:223], v[234:235], off offset:256
	v_add_u32_e32 v232, 16, v232
	v_ashrrev_i32_e32 v233, 31, v232
	v_lshlrev_b64 v[234:235], 12, v[232:233]
	v_lshl_add_u64 v[234:235], v[132:133], 0, v[234:235]
	global_load_dwordx4 v[224:227], v[234:235], off
	global_load_dwordx4 v[228:231], v[234:235], off offset:256
	s_waitcnt vmcnt(0)
	v_lshlrev_b32_e32 v154, 16, v134
	v_and_b32_e32 v155, 0xffff0000, v134
	v_lshlrev_b32_e32 v134, 16, v135
	v_and_b32_e32 v135, 0xffff0000, v135
	v_lshlrev_b32_e32 v188, 16, v136
	v_and_b32_e32 v189, 0xffff0000, v136
	v_lshlrev_b32_e32 v136, 16, v137
	v_and_b32_e32 v137, 0xffff0000, v137
	v_lshlrev_b32_e32 v190, 16, v138
	v_and_b32_e32 v191, 0xffff0000, v138
	v_lshlrev_b32_e32 v138, 16, v139
	v_and_b32_e32 v139, 0xffff0000, v139
	v_lshlrev_b32_e32 v192, 16, v140
	v_and_b32_e32 v193, 0xffff0000, v140
	v_lshlrev_b32_e32 v140, 16, v141
	v_and_b32_e32 v141, 0xffff0000, v141
	v_pk_mul_f32 v[130:131], v[130:131], v[134:135]
	v_pk_mul_f32 v[126:127], v[126:127], v[136:137]
	v_pk_mul_f32 v[122:123], v[122:123], v[138:139]
	v_pk_mul_f32 v[118:119], v[118:119], v[140:141]
	v_lshlrev_b32_e32 v134, 16, v142
	v_and_b32_e32 v135, 0xffff0000, v142
	v_lshlrev_b32_e32 v136, 16, v143
	v_and_b32_e32 v137, 0xffff0000, v143
	v_lshlrev_b32_e32 v138, 16, v144
	v_and_b32_e32 v139, 0xffff0000, v144
	v_lshlrev_b32_e32 v140, 16, v145
	v_and_b32_e32 v141, 0xffff0000, v145
	v_pk_mul_f32 v[128:129], v[128:129], v[154:155]
	v_pk_mul_f32 v[124:125], v[124:125], v[188:189]
	v_pk_mul_f32 v[120:121], v[120:121], v[190:191]
	v_pk_mul_f32 v[116:117], v[116:117], v[192:193]
	v_lshlrev_b32_e32 v142, 16, v146
	v_and_b32_e32 v143, 0xffff0000, v146
	v_lshlrev_b32_e32 v144, 16, v147
	v_and_b32_e32 v145, 0xffff0000, v147
	v_lshlrev_b32_e32 v146, 16, v148
	v_and_b32_e32 v147, 0xffff0000, v148
	v_lshlrev_b32_e32 v148, 16, v149
	v_and_b32_e32 v149, 0xffff0000, v149
	v_lshlrev_b32_e32 v154, 16, v150
	v_and_b32_e32 v155, 0xffff0000, v150
	v_pk_mul_f32 v[114:115], v[114:115], v[136:137]
	v_pk_mul_f32 v[112:113], v[112:113], v[134:135]
	v_pk_mul_f32 v[110:111], v[110:111], v[140:141]
	v_pk_mul_f32 v[108:109], v[108:109], v[138:139]
	v_lshlrev_b32_e32 v134, 16, v176
	v_and_b32_e32 v135, 0xffff0000, v176
	v_lshlrev_b32_e32 v136, 16, v177
	v_and_b32_e32 v137, 0xffff0000, v177
	v_lshlrev_b32_e32 v138, 16, v178
	v_and_b32_e32 v139, 0xffff0000, v178
	v_lshlrev_b32_e32 v140, 16, v179
	v_and_b32_e32 v141, 0xffff0000, v179
	v_lshlrev_b32_e32 v150, 16, v151
	v_and_b32_e32 v151, 0xffff0000, v151
	v_lshlrev_b32_e32 v188, 16, v152
	v_and_b32_e32 v189, 0xffff0000, v152
	v_lshlrev_b32_e32 v152, 16, v153
	v_and_b32_e32 v153, 0xffff0000, v153
	v_pk_mul_f32 v[106:107], v[106:107], v[144:145]
	v_pk_mul_f32 v[104:105], v[104:105], v[142:143]
	v_pk_mul_f32 v[102:103], v[102:103], v[148:149]
	v_pk_mul_f32 v[100:101], v[100:101], v[146:147]
	v_pk_mul_f32 v[96:97], v[96:97], v[154:155]
	v_pk_mul_f32 v[90:91], v[90:91], v[136:137]
	v_pk_mul_f32 v[88:89], v[88:89], v[134:135]
	v_pk_mul_f32 v[86:87], v[86:87], v[140:141]
	v_pk_mul_f32 v[84:85], v[84:85], v[138:139]
	v_lshlrev_b32_e32 v134, 16, v180
	v_and_b32_e32 v135, 0xffff0000, v180
	v_lshlrev_b32_e32 v136, 16, v181
	v_and_b32_e32 v137, 0xffff0000, v181
	v_lshlrev_b32_e32 v138, 16, v182
	v_and_b32_e32 v139, 0xffff0000, v182
	v_lshlrev_b32_e32 v140, 16, v183
	v_and_b32_e32 v141, 0xffff0000, v183
	v_add_u32_e32 v154, s83, v3
	v_pk_mul_f32 v[98:99], v[98:99], v[150:151]
	v_pk_mul_f32 v[94:95], v[94:95], v[152:153]
	v_pk_mul_f32 v[92:93], v[92:93], v[188:189]
	v_pk_mul_f32 v[82:83], v[82:83], v[136:137]
	v_pk_mul_f32 v[80:81], v[80:81], v[134:135]
	v_pk_mul_f32 v[78:79], v[78:79], v[140:141]
	v_pk_mul_f32 v[76:77], v[76:77], v[138:139]
	v_lshlrev_b32_e32 v134, 16, v184
	v_and_b32_e32 v135, 0xffff0000, v184
	v_lshlrev_b32_e32 v136, 16, v185
	v_and_b32_e32 v137, 0xffff0000, v185
	v_lshlrev_b32_e32 v138, 16, v186
	v_and_b32_e32 v139, 0xffff0000, v186
	v_lshlrev_b32_e32 v140, 16, v187
	v_and_b32_e32 v141, 0xffff0000, v187
	v_ashrrev_i32_e32 v155, 31, v154
	v_pk_mul_f32 v[74:75], v[74:75], v[136:137]
	v_pk_mul_f32 v[72:73], v[72:73], v[134:135]
	v_pk_mul_f32 v[70:71], v[70:71], v[140:141]
	v_pk_mul_f32 v[68:69], v[68:69], v[138:139]
	v_lshlrev_b64 v[134:135], 12, v[154:155]
	v_add_u32_e32 v142, 16, v154
	v_lshl_add_u64 v[138:139], v[132:133], 0, v[134:135]
	v_ashrrev_i32_e32 v143, 31, v142
	v_mov_b64_e32 v[134:135], v[200:201]
	v_mov_b64_e32 v[136:137], v[202:203]
	s_nop 0
	v_mov_b64_e32 v[138:139], v[204:205]
	v_mov_b64_e32 v[140:141], v[206:207]
	v_lshlrev_b64 v[142:143], 12, v[142:143]
	v_add_u32_e32 v150, 32, v154
	v_lshl_add_u64 v[146:147], v[132:133], 0, v[142:143]
	v_ashrrev_i32_e32 v151, 31, v150
	v_mov_b64_e32 v[142:143], v[208:209]
	v_mov_b64_e32 v[144:145], v[210:211]
	s_nop 0
	v_mov_b64_e32 v[146:147], v[212:213]
	v_mov_b64_e32 v[148:149], v[214:215]
	v_lshlrev_b64 v[150:151], 12, v[150:151]
	v_add_u32_e32 v154, 48, v154
	v_lshl_add_u64 v[176:177], v[132:133], 0, v[150:151]
	v_ashrrev_i32_e32 v155, 31, v154
	v_mov_b64_e32 v[150:151], v[216:217]
	v_mov_b64_e32 v[152:153], v[218:219]
	s_nop 0
	v_mov_b64_e32 v[176:177], v[220:221]
	v_mov_b64_e32 v[178:179], v[222:223]
	v_lshlrev_b64 v[154:155], 12, v[154:155]
	v_lshl_add_u64 v[132:133], v[132:133], 0, v[154:155]
	v_mov_b64_e32 v[180:181], v[224:225]
	v_mov_b64_e32 v[182:183], v[226:227]
	v_mov_b64_e32 v[184:185], v[228:229]
	v_mov_b64_e32 v[186:187], v[230:231]
	v_lshlrev_b32_e32 v132, 16, v134
	v_and_b32_e32 v133, 0xffff0000, v134
	v_lshlrev_b32_e32 v134, 16, v135
	v_and_b32_e32 v135, 0xffff0000, v135
	v_lshlrev_b32_e32 v154, 16, v136
	v_and_b32_e32 v155, 0xffff0000, v136
	v_lshlrev_b32_e32 v136, 16, v137
	v_and_b32_e32 v137, 0xffff0000, v137
	v_lshlrev_b32_e32 v188, 16, v138
	v_and_b32_e32 v189, 0xffff0000, v138
	v_lshlrev_b32_e32 v138, 16, v139
	v_and_b32_e32 v139, 0xffff0000, v139
	v_pk_mul_f32 v[58:59], v[58:59], v[134:135]
	v_pk_mul_f32 v[56:57], v[56:57], v[132:133]
	v_pk_mul_f32 v[54:55], v[54:55], v[136:137]
	v_pk_mul_f32 v[66:67], v[66:67], v[138:139]
	v_lshlrev_b32_e32 v132, 16, v142
	v_and_b32_e32 v133, 0xffff0000, v142
	v_lshlrev_b32_e32 v134, 16, v143
	v_and_b32_e32 v135, 0xffff0000, v143
	v_lshlrev_b32_e32 v136, 16, v144
	v_and_b32_e32 v137, 0xffff0000, v144
	v_lshlrev_b32_e32 v138, 16, v145
	v_and_b32_e32 v139, 0xffff0000, v145
	v_pk_mul_f32 v[50:51], v[50:51], v[134:135]
	v_pk_mul_f32 v[48:49], v[48:49], v[132:133]
	v_pk_mul_f32 v[46:47], v[46:47], v[138:139]
	v_pk_mul_f32 v[44:45], v[44:45], v[136:137]
	v_lshlrev_b32_e32 v132, 16, v146
	v_and_b32_e32 v133, 0xffff0000, v146
	v_lshlrev_b32_e32 v134, 16, v147
	v_and_b32_e32 v135, 0xffff0000, v147
	v_lshlrev_b32_e32 v136, 16, v148
	v_and_b32_e32 v137, 0xffff0000, v148
	v_lshlrev_b32_e32 v138, 16, v149
	v_and_b32_e32 v139, 0xffff0000, v149
	v_lshlrev_b32_e32 v190, 16, v140
	v_and_b32_e32 v191, 0xffff0000, v140
	v_lshlrev_b32_e32 v140, 16, v141
	v_and_b32_e32 v141, 0xffff0000, v141
	v_pk_mul_f32 v[42:43], v[42:43], v[134:135]
	v_pk_mul_f32 v[40:41], v[40:41], v[132:133]
	v_pk_mul_f32 v[38:39], v[38:39], v[138:139]
	v_pk_mul_f32 v[36:37], v[36:37], v[136:137]
	v_lshlrev_b32_e32 v132, 16, v150
	v_and_b32_e32 v133, 0xffff0000, v150
	v_lshlrev_b32_e32 v134, 16, v151
	v_and_b32_e32 v135, 0xffff0000, v151
	v_lshlrev_b32_e32 v136, 16, v152
	v_and_b32_e32 v137, 0xffff0000, v152
	v_lshlrev_b32_e32 v138, 16, v153
	v_and_b32_e32 v139, 0xffff0000, v153
	v_pk_mul_f32 v[52:53], v[52:53], v[154:155]
	v_pk_mul_f32 v[64:65], v[64:65], v[188:189]
	v_pk_mul_f32 v[62:63], v[62:63], v[140:141]
	v_pk_mul_f32 v[60:61], v[60:61], v[190:191]
	v_pk_mul_f32 v[34:35], v[34:35], v[134:135]
	v_pk_mul_f32 v[32:33], v[32:33], v[132:133]
	v_pk_mul_f32 v[30:31], v[30:31], v[138:139]
	v_pk_mul_f32 v[28:29], v[28:29], v[136:137]
	v_lshlrev_b32_e32 v132, 16, v176
	v_and_b32_e32 v133, 0xffff0000, v176
	v_lshlrev_b32_e32 v134, 16, v177
	v_and_b32_e32 v135, 0xffff0000, v177
	v_lshlrev_b32_e32 v136, 16, v178
	v_and_b32_e32 v137, 0xffff0000, v178
	v_lshlrev_b32_e32 v138, 16, v179
	v_and_b32_e32 v139, 0xffff0000, v179
	v_pk_mul_f32 v[26:27], v[26:27], v[134:135]
	v_pk_mul_f32 v[24:25], v[24:25], v[132:133]
	v_pk_mul_f32 v[22:23], v[22:23], v[138:139]
	v_pk_mul_f32 v[20:21], v[20:21], v[136:137]
	v_lshlrev_b32_e32 v132, 16, v180
	v_and_b32_e32 v133, 0xffff0000, v180
	v_lshlrev_b32_e32 v134, 16, v181
	v_and_b32_e32 v135, 0xffff0000, v181
	v_lshlrev_b32_e32 v136, 16, v182
	v_and_b32_e32 v137, 0xffff0000, v182
	v_lshlrev_b32_e32 v138, 16, v183
	v_and_b32_e32 v139, 0xffff0000, v183
	v_pk_mul_f32 v[18:19], v[18:19], v[134:135]
	v_pk_mul_f32 v[16:17], v[16:17], v[132:133]
	v_pk_mul_f32 v[14:15], v[14:15], v[138:139]
	v_pk_mul_f32 v[12:13], v[12:13], v[136:137]
	v_lshlrev_b32_e32 v132, 16, v184
	v_and_b32_e32 v133, 0xffff0000, v184
	v_lshlrev_b32_e32 v134, 16, v185
	v_and_b32_e32 v135, 0xffff0000, v185
	v_lshlrev_b32_e32 v136, 16, v186
	v_and_b32_e32 v137, 0xffff0000, v186
	v_lshlrev_b32_e32 v138, 16, v187
	v_and_b32_e32 v139, 0xffff0000, v187
	v_pk_mul_f32 v[10:11], v[10:11], v[134:135]
	v_pk_mul_f32 v[8:9], v[8:9], v[132:133]
	v_pk_mul_f32 v[6:7], v[6:7], v[138:139]
	v_pk_mul_f32 v[4:5], v[4:5], v[136:137]
	s_nop 0
	s_branch .LBB0_961

.LBB0_966:
	v_mov_b32_e32 v3, 0
	v_mov_b32_e32 v132, 0
	s_or_b32 s2, s52, s67
	v_add_u32_e32 v199, v132, v1
	v_add3_u32 v178, s31, v194, v3
	v_lshlrev_b32_e32 v176, 3, v199
	s_add_u32 s42, s74, s54
	v_ashrrev_i32_e32 v177, 31, v176
	s_addc_u32 s43, s75, s55
	v_ashrrev_i32_e32 v179, 31, v178
	v_lshl_add_u64 v[180:181], v[176:177], 1, s[42:43]
	v_lshlrev_b64 v[208:209], 12, v[178:179]
	v_lshl_add_u64 v[132:133], v[180:181], 0, v[208:209]
	global_load_dwordx4 v[200:203], v[132:133], off
	global_load_dwordx4 v[204:207], v[132:133], off offset:256
	v_add_u32_e32 v190, 16, v178
	v_add_u32_e32 v186, 32, v178
	v_add_u32_e32 v182, 48, v178
	v_ashrrev_i32_e32 v191, 31, v190
	v_ashrrev_i32_e32 v187, 31, v186
	v_ashrrev_i32_e32 v183, 31, v182
	v_lshlrev_b64 v[192:193], 12, v[190:191]
	v_lshlrev_b64 v[188:189], 12, v[186:187]
	v_lshlrev_b64 v[184:185], 12, v[182:183]
	v_lshl_add_u64 v[132:133], v[180:181], 0, v[192:193]
	v_lshl_add_u64 v[134:135], v[180:181], 0, v[188:189]
	v_lshl_add_u64 v[210:211], v[180:181], 0, v[184:185]
	global_load_dwordx4 v[152:155], v[132:133], off
	global_load_dwordx4 v[148:151], v[132:133], off offset:256
	global_load_dwordx4 v[144:147], v[134:135], off
	global_load_dwordx4 v[140:143], v[134:135], off offset:256
	global_load_dwordx4 v[136:139], v[210:211], off
	s_nop 0
	global_load_dwordx4 v[132:135], v[210:211], off offset:256
	v_add_u32_e32 v250, 0x80, v178
	v_ashrrev_i32_e32 v251, 31, v250
	v_lshlrev_b64 v[252:253], 12, v[250:251]
	v_lshl_add_u64 v[252:253], v[180:181], 0, v[252:253]
	global_load_dwordx4 v[218:221], v[252:253], off
	global_load_dwordx4 v[222:225], v[252:253], off offset:256
	v_add_u32_e32 v250, 0x90, v178
	v_ashrrev_i32_e32 v251, 31, v250
	v_lshlrev_b64 v[252:253], 12, v[250:251]
	v_lshl_add_u64 v[252:253], v[180:181], 0, v[252:253]
	global_load_dwordx4 v[226:229], v[252:253], off
	global_load_dwordx4 v[230:233], v[252:253], off offset:256
	v_add_u32_e32 v250, 0xa0, v178
	v_ashrrev_i32_e32 v251, 31, v250
	v_lshlrev_b64 v[252:253], 12, v[250:251]
	v_lshl_add_u64 v[252:253], v[180:181], 0, v[252:253]
	global_load_dwordx4 v[234:237], v[252:253], off
	global_load_dwordx4 v[238:241], v[252:253], off offset:256
	v_add_u32_e32 v250, 0xb0, v178
	v_ashrrev_i32_e32 v251, 31, v250
	v_lshlrev_b64 v[252:253], 12, v[250:251]
	v_lshl_add_u64 v[252:253], v[180:181], 0, v[252:253]
	global_load_dwordx4 v[242:245], v[252:253], off
	global_load_dwordx4 v[246:249], v[252:253], off offset:256
	v_add_u32_e32 v176, s2, v176
	v_lshl_add_u64 v[208:209], s[14:15], 0, v[208:209]
	v_ashrrev_i32_e32 v177, 31, v176
	v_cmp_eq_u32_e32 vcc, 0, v199
	s_waitcnt vmcnt(0)
	v_lshlrev_b32_e32 v210, 16, v200
	v_and_b32_e32 v211, 0xffff0000, v200
	v_lshlrev_b32_e32 v212, 16, v202
	v_and_b32_e32 v213, 0xffff0000, v202
	v_lshlrev_b32_e32 v200, 16, v201
	v_and_b32_e32 v201, 0xffff0000, v201
	v_lshlrev_b32_e32 v202, 16, v203
	v_and_b32_e32 v203, 0xffff0000, v203
	v_lshlrev_b32_e32 v216, 16, v206
	v_and_b32_e32 v217, 0xffff0000, v206
	v_lshlrev_b32_e32 v206, 16, v207
	v_and_b32_e32 v207, 0xffff0000, v207
	v_pk_mul_f32 v[128:129], v[128:129], v[210:211]
	v_pk_mul_f32 v[124:125], v[124:125], v[212:213]
	v_lshlrev_b32_e32 v214, 16, v204
	v_and_b32_e32 v215, 0xffff0000, v204
	v_pk_mul_f32 v[130:131], v[130:131], v[200:201]
	v_pk_mul_f32 v[126:127], v[126:127], v[202:203]
	v_pk_mul_f32 v[200:201], v[118:119], v[206:207]
	v_pk_mul_f32 v[202:203], v[116:117], v[216:217]
	v_cvt_pk_bf16_f32 v116, v128, v129
	v_cvt_pk_bf16_f32 v117, v130, v131
	v_cvt_pk_bf16_f32 v118, v124, v125
	v_max_f32_e64 v3, |v128|, |v124|
	v_max_f32_e64 v124, |v129|, |v125|
	v_lshlrev_b32_e32 v204, 16, v205
	v_and_b32_e32 v205, 0xffff0000, v205
	v_pk_mul_f32 v[120:121], v[120:121], v[214:215]
	v_cvt_pk_bf16_f32 v119, v126, v127
	v_max_f32_e64 v125, |v130|, |v126|
	v_max_f32_e64 v126, |v131|, |v127|
	v_max3_f32 v3, v3, 0, v124
	v_pk_mul_f32 v[122:123], v[122:123], v[204:205]
	v_max_f32_e64 v127, |v120|, |v202|
	v_max_f32_e64 v128, |v121|, |v203|
	v_max3_f32 v3, v3, v125, v126
	v_max_f32_e64 v129, |v122|, |v200|
	v_max3_f32 v3, v3, v127, v128
	v_max_f32_e64 v124, |v123|, |v201|
	v_max3_f32 v3, v3, v129, v124
	ds_bpermute_b32 v126, v196, v3
	v_lshl_add_u64 v[124:125], v[176:177], 1, v[208:209]
	global_store_dwordx4 v[124:125], v[116:119], off
	s_waitcnt lgkmcnt(0)
	s_nop 0
	v_max_f32_e32 v116, v126, v126
	v_max_f32_e32 v3, v3, v116
	ds_bpermute_b32 v116, v197, v3
	v_cvt_pk_bf16_f32 v118, v120, v121
	v_cvt_pk_bf16_f32 v119, v122, v123
	v_cvt_pk_bf16_f32 v120, v202, v203
	v_cvt_pk_bf16_f32 v121, v200, v201
	global_store_dwordx4 v[124:125], v[118:121], off offset:256
	s_and_saveexec_b64 s[48:49], vcc
	s_cbranch_execz .LBB0_968
	s_waitcnt lgkmcnt(0)
	v_max_f32_e32 v116, v116, v116
	v_max_f32_e32 v3, v3, v3
	v_lshl_add_u64 v[118:119], v[178:179], 2, s[10:11]
	v_max_f32_e32 v3, v3, v116
	global_atomic_umax v[118:119], v3, off

.LBB0_974:
	s_or_b64 exec, exec, s[48:49]
	v_add_u32_e32 v104, 0x80, v178
	v_ashrrev_i32_e32 v105, 31, v104
	v_lshlrev_b64 v[114:115], 12, v[104:105]
	s_waitcnt lgkmcnt(0)
	v_lshl_add_u64 v[68:69], v[180:181], 0, v[114:115]
	v_mov_b64_e32 v[106:107], v[218:219]
	v_mov_b64_e32 v[108:109], v[220:221]
	v_mov_b64_e32 v[110:111], v[222:223]
	v_mov_b64_e32 v[112:113], v[224:225]
	v_add_u32_e32 v100, 0x90, v178
	v_add_u32_e32 v96, 0xa0, v178
	v_add_u32_e32 v92, 0xb0, v178
	v_ashrrev_i32_e32 v101, 31, v100
	v_ashrrev_i32_e32 v97, 31, v96
	v_ashrrev_i32_e32 v93, 31, v92
	v_lshlrev_b64 v[102:103], 12, v[100:101]
	v_lshlrev_b64 v[98:99], 12, v[96:97]
	v_lshlrev_b64 v[94:95], 12, v[92:93]
	v_lshl_add_u64 v[68:69], v[180:181], 0, v[102:103]
	v_lshl_add_u64 v[70:71], v[180:181], 0, v[98:99]
	v_lshl_add_u64 v[116:117], v[180:181], 0, v[94:95]
	v_mov_b64_e32 v[88:89], v[226:227]
	v_mov_b64_e32 v[90:91], v[228:229]
	v_mov_b64_e32 v[84:85], v[230:231]
	v_mov_b64_e32 v[86:87], v[232:233]
	v_mov_b64_e32 v[80:81], v[234:235]
	v_mov_b64_e32 v[82:83], v[236:237]
	v_mov_b64_e32 v[76:77], v[238:239]
	v_mov_b64_e32 v[78:79], v[240:241]
	v_mov_b64_e32 v[72:73], v[242:243]
	v_mov_b64_e32 v[74:75], v[244:245]
	s_nop 0
	v_mov_b64_e32 v[68:69], v[246:247]
	v_mov_b64_e32 v[70:71], v[248:249]
	v_lshlrev_b32_e32 v116, 16, v106
	v_and_b32_e32 v117, 0xffff0000, v106
	v_lshlrev_b32_e32 v106, 16, v107
	v_and_b32_e32 v107, 0xffff0000, v107
	v_lshlrev_b32_e32 v118, 16, v108
	v_and_b32_e32 v119, 0xffff0000, v108
	v_lshlrev_b32_e32 v108, 16, v109
	v_and_b32_e32 v109, 0xffff0000, v109
	v_pk_mul_f32 v[58:59], v[58:59], v[106:107]
	v_pk_mul_f32 v[56:57], v[56:57], v[116:117]
	v_pk_mul_f32 v[106:107], v[54:55], v[108:109]
	v_pk_mul_f32 v[108:109], v[52:53], v[118:119]
	v_lshlrev_b32_e32 v120, 16, v110
	v_and_b32_e32 v121, 0xffff0000, v110
	v_lshlrev_b32_e32 v122, 16, v112
	v_and_b32_e32 v123, 0xffff0000, v112
	v_cvt_pk_bf16_f32 v52, v56, v57
	v_max_f32_e64 v3, |v56|, |v108|
	v_max_f32_e64 v56, |v57|, |v109|
	v_lshlrev_b32_e32 v110, 16, v111
	v_and_b32_e32 v111, 0xffff0000, v111
	v_lshlrev_b32_e32 v112, 16, v113
	v_and_b32_e32 v113, 0xffff0000, v113
	v_pk_mul_f32 v[64:65], v[64:65], v[120:121]
	v_pk_mul_f32 v[60:61], v[60:61], v[122:123]
	v_cvt_pk_bf16_f32 v53, v58, v59
	v_max_f32_e64 v57, |v58|, |v106|
	v_max_f32_e64 v58, |v59|, |v107|
	v_max3_f32 v3, v3, 0, v56
	v_pk_mul_f32 v[66:67], v[66:67], v[110:111]
	v_pk_mul_f32 v[62:63], v[62:63], v[112:113]
	v_cvt_pk_bf16_f32 v54, v108, v109
	v_cvt_pk_bf16_f32 v55, v106, v107
	v_max_f32_e64 v59, |v64|, |v60|
	v_max_f32_e64 v106, |v65|, |v61|
	v_max3_f32 v3, v3, v57, v58
	v_max_f32_e64 v107, |v66|, |v62|
	v_max3_f32 v3, v3, v59, v106
	v_max_f32_e64 v56, |v67|, |v63|
	v_max3_f32 v3, v3, v107, v56
	ds_bpermute_b32 v106, v196, v3
	v_lshl_add_u64 v[56:57], s[14:15], 0, v[114:115]
	v_lshl_add_u64 v[58:59], v[176:177], 1, v[56:57]
	global_store_dwordx4 v[58:59], v[52:55], off
	s_waitcnt lgkmcnt(0)
	s_nop 0
	v_max_f32_e32 v52, v106, v106
	v_max_f32_e32 v3, v3, v52
	ds_bpermute_b32 v52, v197, v3
	v_cvt_pk_bf16_f32 v54, v64, v65
	v_cvt_pk_bf16_f32 v55, v66, v67
	v_cvt_pk_bf16_f32 v56, v60, v61
	v_cvt_pk_bf16_f32 v57, v62, v63
	global_store_dwordx4 v[58:59], v[54:57], off offset:256
	s_and_saveexec_b64 s[48:49], vcc
	s_cbranch_execz .LBB0_976
	s_waitcnt lgkmcnt(0)
	v_max_f32_e32 v52, v52, v52
	v_max_f32_e32 v3, v3, v3
	v_lshl_add_u64 v[54:55], v[104:105], 2, s[10:11]
	v_max_f32_e32 v3, v3, v52
	global_atomic_umax v[54:55], v3, off
.LBB0_976:
	s_or_b64 exec, exec, s[48:49]
	s_waitcnt lgkmcnt(0)
	v_lshlrev_b32_e32 v52, 16, v88
	v_and_b32_e32 v53, 0xffff0000, v88
	v_lshlrev_b32_e32 v54, 16, v89
	v_and_b32_e32 v55, 0xffff0000, v89
	v_lshlrev_b32_e32 v56, 16, v90
	v_and_b32_e32 v57, 0xffff0000, v90
	v_lshlrev_b32_e32 v58, 16, v91
	v_and_b32_e32 v59, 0xffff0000, v91
	v_pk_mul_f32 v[50:51], v[50:51], v[54:55]
	v_pk_mul_f32 v[48:49], v[48:49], v[52:53]
	v_pk_mul_f32 v[54:55], v[44:45], v[56:57]
	v_pk_mul_f32 v[52:53], v[46:47], v[58:59]
	v_cvt_pk_bf16_f32 v44, v48, v49
	v_max_f32_e64 v3, |v48|, |v54|
	v_max_f32_e64 v48, |v49|, |v55|
	v_max3_f32 v3, v3, 0, v48
	v_max_f32_e64 v48, |v50|, |v52|
	v_max_f32_e64 v49, |v51|, |v53|
	v_cvt_pk_bf16_f32 v45, v50, v51
	v_cvt_pk_bf16_f32 v46, v54, v55
	v_cvt_pk_bf16_f32 v47, v52, v53
	v_max3_f32 v3, v3, v48, v49
	v_lshlrev_b32_e32 v48, 16, v84
	v_and_b32_e32 v49, 0xffff0000, v84
	v_lshlrev_b32_e32 v50, 16, v85
	v_and_b32_e32 v51, 0xffff0000, v85
	v_lshlrev_b32_e32 v52, 16, v86
	v_and_b32_e32 v53, 0xffff0000, v86
	v_lshlrev_b32_e32 v54, 16, v87
	v_and_b32_e32 v55, 0xffff0000, v87
	v_pk_mul_f32 v[42:43], v[42:43], v[50:51]
	v_pk_mul_f32 v[40:41], v[40:41], v[48:49]
	v_pk_mul_f32 v[50:51], v[36:37], v[52:53]
	v_pk_mul_f32 v[48:49], v[38:39], v[54:55]
	v_max_f32_e64 v36, |v40|, |v50|
	v_max_f32_e64 v37, |v41|, |v51|
	v_max3_f32 v3, v3, v36, v37
	v_max_f32_e64 v36, |v42|, |v48|
	v_max_f32_e64 v37, |v43|, |v49|
	v_max3_f32 v3, v3, v36, v37
	ds_bpermute_b32 v39, v196, v3
	v_lshl_add_u64 v[36:37], s[14:15], 0, v[102:103]
	v_lshl_add_u64 v[52:53], v[176:177], 1, v[36:37]
	global_store_dwordx4 v[52:53], v[44:47], off
	v_cvt_pk_bf16_f32 v38, v40, v41
	s_waitcnt lgkmcnt(0)
	v_max_f32_e32 v36, v39, v39
	v_max_f32_e32 v3, v3, v36
	ds_bpermute_b32 v36, v197, v3
	v_cvt_pk_bf16_f32 v39, v42, v43
	v_cvt_pk_bf16_f32 v40, v50, v51
	v_cvt_pk_bf16_f32 v41, v48, v49
	global_store_dwordx4 v[52:53], v[38:41], off offset:256
	s_and_saveexec_b64 s[48:49], vcc
	s_cbranch_execz .LBB0_978
	s_waitcnt lgkmcnt(0)
	v_max_f32_e32 v36, v36, v36
	v_max_f32_e32 v3, v3, v3
	v_lshl_add_u64 v[38:39], v[100:101], 2, s[10:11]
	v_max_f32_e32 v3, v3, v36
	global_atomic_umax v[38:39], v3, off
.LBB0_978:
	s_or_b64 exec, exec, s[48:49]
	s_waitcnt lgkmcnt(0)
	v_lshlrev_b32_e32 v36, 16, v80
	v_and_b32_e32 v37, 0xffff0000, v80
	v_lshlrev_b32_e32 v38, 16, v81
	v_and_b32_e32 v39, 0xffff0000, v81
	v_lshlrev_b32_e32 v40, 16, v82
	v_and_b32_e32 v41, 0xffff0000, v82
	v_lshlrev_b32_e32 v42, 16, v83
	v_and_b32_e32 v43, 0xffff0000, v83
	v_pk_mul_f32 v[34:35], v[34:35], v[38:39]
	v_pk_mul_f32 v[32:33], v[32:33], v[36:37]
	v_pk_mul_f32 v[38:39], v[28:29], v[40:41]
	v_pk_mul_f32 v[36:37], v[30:31], v[42:43]
	v_cvt_pk_bf16_f32 v28, v32, v33
	v_max_f32_e64 v3, |v32|, |v38|
	v_max_f32_e64 v32, |v33|, |v39|
	v_max3_f32 v3, v3, 0, v32
	v_max_f32_e64 v32, |v34|, |v36|
	v_max_f32_e64 v33, |v35|, |v37|
	v_cvt_pk_bf16_f32 v29, v34, v35
	v_cvt_pk_bf16_f32 v30, v38, v39
	v_cvt_pk_bf16_f32 v31, v36, v37
	v_max3_f32 v3, v3, v32, v33
	v_lshlrev_b32_e32 v32, 16, v76
	v_and_b32_e32 v33, 0xffff0000, v76
	v_lshlrev_b32_e32 v34, 16, v77
	v_and_b32_e32 v35, 0xffff0000, v77
	v_lshlrev_b32_e32 v36, 16, v78
	v_and_b32_e32 v37, 0xffff0000, v78
	v_lshlrev_b32_e32 v38, 16, v79
	v_and_b32_e32 v39, 0xffff0000, v79
	v_pk_mul_f32 v[26:27], v[26:27], v[34:35]
	v_pk_mul_f32 v[24:25], v[24:25], v[32:33]
	v_pk_mul_f32 v[34:35], v[20:21], v[36:37]
	v_pk_mul_f32 v[32:33], v[22:23], v[38:39]
	v_max_f32_e64 v20, |v24|, |v34|
	v_max_f32_e64 v21, |v25|, |v35|
	v_max3_f32 v3, v3, v20, v21
	v_max_f32_e64 v20, |v26|, |v32|
	v_max_f32_e64 v21, |v27|, |v33|
	v_max3_f32 v3, v3, v20, v21
	ds_bpermute_b32 v23, v196, v3
	v_lshl_add_u64 v[20:21], s[14:15], 0, v[98:99]
	v_lshl_add_u64 v[36:37], v[176:177], 1, v[20:21]
	global_store_dwordx4 v[36:37], v[28:31], off
	v_cvt_pk_bf16_f32 v22, v24, v25
	s_waitcnt lgkmcnt(0)
	v_max_f32_e32 v20, v23, v23
	v_max_f32_e32 v3, v3, v20
	ds_bpermute_b32 v20, v197, v3
	v_cvt_pk_bf16_f32 v23, v26, v27
	v_cvt_pk_bf16_f32 v24, v34, v35
	v_cvt_pk_bf16_f32 v25, v32, v33
	global_store_dwordx4 v[36:37], v[22:25], off offset:256
	s_and_saveexec_b64 s[48:49], vcc
	s_cbranch_execz .LBB0_980
	s_waitcnt lgkmcnt(0)
	v_max_f32_e32 v20, v20, v20
	v_max_f32_e32 v3, v3, v3
	v_lshl_add_u64 v[22:23], v[96:97], 2, s[10:11]
	v_max_f32_e32 v3, v3, v20
	global_atomic_umax v[22:23], v3, off
.LBB0_980:
	s_or_b64 exec, exec, s[48:49]
	s_waitcnt lgkmcnt(0)
	v_lshlrev_b32_e32 v20, 16, v72
	v_and_b32_e32 v21, 0xffff0000, v72
	v_lshlrev_b32_e32 v22, 16, v73
	v_and_b32_e32 v23, 0xffff0000, v73
	v_lshlrev_b32_e32 v24, 16, v74
	v_and_b32_e32 v25, 0xffff0000, v74
	v_lshlrev_b32_e32 v26, 16, v75
	v_and_b32_e32 v27, 0xffff0000, v75
	v_pk_mul_f32 v[18:19], v[18:19], v[22:23]
	v_pk_mul_f32 v[16:17], v[16:17], v[20:21]
	v_pk_mul_f32 v[22:23], v[12:13], v[24:25]
	v_pk_mul_f32 v[20:21], v[14:15], v[26:27]
	v_cvt_pk_bf16_f32 v12, v16, v17
	v_max_f32_e64 v3, |v16|, |v22|
	v_max_f32_e64 v16, |v17|, |v23|
	v_max3_f32 v3, v3, 0, v16
	v_max_f32_e64 v16, |v18|, |v20|
	v_max_f32_e64 v17, |v19|, |v21|
	v_cvt_pk_bf16_f32 v13, v18, v19
	v_cvt_pk_bf16_f32 v14, v22, v23
	v_cvt_pk_bf16_f32 v15, v20, v21
	v_max3_f32 v3, v3, v16, v17
	v_lshlrev_b32_e32 v16, 16, v68
	v_and_b32_e32 v17, 0xffff0000, v68
	v_lshlrev_b32_e32 v18, 16, v69
	v_and_b32_e32 v19, 0xffff0000, v69
	v_lshlrev_b32_e32 v20, 16, v70
	v_and_b32_e32 v21, 0xffff0000, v70
	v_lshlrev_b32_e32 v22, 16, v71
	v_and_b32_e32 v23, 0xffff0000, v71
	v_pk_mul_f32 v[10:11], v[10:11], v[18:19]
	v_pk_mul_f32 v[8:9], v[8:9], v[16:17]
	v_pk_mul_f32 v[18:19], v[4:5], v[20:21]
	v_pk_mul_f32 v[16:17], v[6:7], v[22:23]
	v_max_f32_e64 v4, |v8|, |v18|
	v_max_f32_e64 v5, |v9|, |v19|
	v_max3_f32 v3, v3, v4, v5
	v_max_f32_e64 v4, |v10|, |v16|
	v_max_f32_e64 v5, |v11|, |v17|
	v_max3_f32 v3, v3, v4, v5
	ds_bpermute_b32 v7, v196, v3
	v_lshl_add_u64 v[4:5], s[14:15], 0, v[94:95]
	v_lshl_add_u64 v[20:21], v[176:177], 1, v[4:5]
	global_store_dwordx4 v[20:21], v[12:15], off
	v_cvt_pk_bf16_f32 v6, v8, v9
	s_waitcnt lgkmcnt(0)
	v_max_f32_e32 v4, v7, v7
	v_max_f32_e32 v3, v3, v4
	ds_bpermute_b32 v4, v197, v3
	v_cvt_pk_bf16_f32 v7, v10, v11
	v_cvt_pk_bf16_f32 v8, v18, v19
	v_cvt_pk_bf16_f32 v9, v16, v17
	global_store_dwordx4 v[20:21], v[6:9], off offset:256
	s_and_saveexec_b64 s[48:49], vcc
	s_cbranch_execz .LBB0_982
	s_waitcnt lgkmcnt(0)
	v_max_f32_e32 v4, v4, v4
	v_max_f32_e32 v3, v3, v3
	v_lshl_add_u64 v[6:7], v[92:93], 2, s[10:11]
	v_max_f32_e32 v3, v3, v4
	global_atomic_umax v[6:7], v3, off
